# MoE K-loops: LDS fragment reads of block n+1 software-pipelined under the MFMAs of block n with counted lgkmcnt waits (full-tile path), half-tile path out of line
# speedup vs baseline: 1.0082x; 1.0082x over previous
.LBB0_726:
	s_cmp_lg_u64 s[2:3], 0
	s_cbranch_scc1 .Lswp_guE_half
	ds_read_b64_tr_b16 v[162:163], v190 offset:0
	ds_read_b64_tr_b16 v[164:165], v191 offset:0
	ds_read_b64_tr_b16 v[166:167], v190 offset:8192
	ds_read_b64_tr_b16 v[168:169], v191 offset:8192
	ds_read_b64_tr_b16 v[170:171], v192 offset:0
	ds_read_b64_tr_b16 v[172:173], v193 offset:0
	ds_read_b64_tr_b16 v[174:175], v192 offset:8192
	ds_read_b64_tr_b16 v[176:177], v193 offset:8192
	ds_read_b128 v[214:217], v207
	ds_read_b128 v[224:227], v207 offset:2048
	ds_read_b128 v[232:235], v207 offset:4096
	ds_read_b128 v[240:243], v207 offset:6144
	ds_read_b128 v[218:221], v207 offset:1024
	ds_read_b128 v[228:231], v207 offset:3072
	ds_read_b128 v[236:239], v207 offset:5120
	ds_read_b128 v[244:247], v207 offset:7168
	s_setprio 1
	s_waitcnt lgkmcnt(7)
	v_mfma_f32_16x16x32_bf16 v[158:161], v[162:165], v[214:217], v[158:161]
	v_mfma_f32_16x16x32_bf16 v[154:157], v[170:173], v[214:217], v[154:157]
	ds_read_b128 v[214:217], v207 offset:16384
	s_waitcnt lgkmcnt(7)
	v_mfma_f32_16x16x32_bf16 v[146:149], v[162:165], v[224:227], v[146:149]
	v_mfma_f32_16x16x32_bf16 v[138:141], v[170:173], v[224:227], v[138:141]
	ds_read_b128 v[224:227], v207 offset:18432
	s_waitcnt lgkmcnt(7)
	v_mfma_f32_16x16x32_bf16 v[130:133], v[162:165], v[232:235], v[130:133]
	v_mfma_f32_16x16x32_bf16 v[122:125], v[170:173], v[232:235], v[122:125]
	ds_read_b128 v[232:235], v207 offset:20480
	s_waitcnt lgkmcnt(7)
	v_mfma_f32_16x16x32_bf16 v[114:117], v[162:165], v[240:243], v[114:117]
	v_mfma_f32_16x16x32_bf16 v[106:109], v[170:173], v[240:243], v[106:109]
	ds_read_b128 v[240:243], v207 offset:22528
	s_waitcnt lgkmcnt(7)
	v_mfma_f32_16x16x32_bf16 v[158:161], v[166:169], v[218:221], v[158:161]
	v_mfma_f32_16x16x32_bf16 v[154:157], v[174:177], v[218:221], v[154:157]
	ds_read_b128 v[218:221], v207 offset:17408
	s_waitcnt lgkmcnt(7)
	v_mfma_f32_16x16x32_bf16 v[146:149], v[166:169], v[228:231], v[146:149]
	v_mfma_f32_16x16x32_bf16 v[138:141], v[174:177], v[228:231], v[138:141]
	ds_read_b128 v[228:231], v207 offset:19456
	s_waitcnt lgkmcnt(7)
	v_mfma_f32_16x16x32_bf16 v[130:133], v[166:169], v[236:239], v[130:133]
	v_mfma_f32_16x16x32_bf16 v[122:125], v[174:177], v[236:239], v[122:125]
	ds_read_b128 v[236:239], v207 offset:21504
	s_waitcnt lgkmcnt(7)
	v_mfma_f32_16x16x32_bf16 v[114:117], v[166:169], v[244:247], v[114:117]
	v_mfma_f32_16x16x32_bf16 v[106:109], v[174:177], v[244:247], v[106:109]
	ds_read_b128 v[244:247], v207 offset:23552
	s_waitcnt lgkmcnt(7)
	v_mfma_f32_16x16x32_bf16 v[94:97], v[162:165], v[214:217], v[94:97]
	v_mfma_f32_16x16x32_bf16 v[86:89], v[170:173], v[214:217], v[86:89]
	ds_read_b128 v[214:217], v207
	s_waitcnt lgkmcnt(7)
	v_mfma_f32_16x16x32_bf16 v[78:81], v[162:165], v[224:227], v[78:81]
	v_mfma_f32_16x16x32_bf16 v[70:73], v[170:173], v[224:227], v[70:73]
	ds_read_b128 v[224:227], v207 offset:2048
	s_waitcnt lgkmcnt(7)
	v_mfma_f32_16x16x32_bf16 v[62:65], v[162:165], v[232:235], v[62:65]
	v_mfma_f32_16x16x32_bf16 v[54:57], v[170:173], v[232:235], v[54:57]
	ds_read_b128 v[232:235], v207 offset:4096
	s_waitcnt lgkmcnt(7)
	v_mfma_f32_16x16x32_bf16 v[46:49], v[162:165], v[240:243], v[46:49]
	v_mfma_f32_16x16x32_bf16 v[38:41], v[170:173], v[240:243], v[38:41]
	ds_read_b128 v[240:243], v207 offset:6144
	ds_read_b64_tr_b16 v[162:163], v190 offset:16384
	ds_read_b64_tr_b16 v[164:165], v191 offset:16384
	ds_read_b64_tr_b16 v[170:171], v192 offset:16384
	ds_read_b64_tr_b16 v[172:173], v193 offset:16384
	s_waitcnt lgkmcnt(11)
	v_mfma_f32_16x16x32_bf16 v[94:97], v[166:169], v[218:221], v[94:97]
	v_mfma_f32_16x16x32_bf16 v[86:89], v[174:177], v[218:221], v[86:89]
	ds_read_b128 v[218:221], v207 offset:1024
	s_waitcnt lgkmcnt(11)
	v_mfma_f32_16x16x32_bf16 v[78:81], v[166:169], v[228:231], v[78:81]
	v_mfma_f32_16x16x32_bf16 v[70:73], v[174:177], v[228:231], v[70:73]
	ds_read_b128 v[228:231], v207 offset:3072
	s_waitcnt lgkmcnt(11)
	v_mfma_f32_16x16x32_bf16 v[62:65], v[166:169], v[236:239], v[62:65]
	v_mfma_f32_16x16x32_bf16 v[54:57], v[174:177], v[236:239], v[54:57]
	ds_read_b128 v[236:239], v207 offset:5120
	s_waitcnt lgkmcnt(11)
	v_mfma_f32_16x16x32_bf16 v[46:49], v[166:169], v[244:247], v[46:49]
	v_mfma_f32_16x16x32_bf16 v[38:41], v[174:177], v[244:247], v[38:41]
	ds_read_b128 v[244:247], v207 offset:7168
	ds_read_b64_tr_b16 v[166:167], v190 offset:24576
	ds_read_b64_tr_b16 v[168:169], v191 offset:24576
	ds_read_b64_tr_b16 v[174:175], v192 offset:24576
	ds_read_b64_tr_b16 v[176:177], v193 offset:24576
	s_waitcnt lgkmcnt(8)
	v_mfma_f32_16x16x32_bf16 v[150:153], v[162:165], v[214:217], v[150:153]
	v_mfma_f32_16x16x32_bf16 v[142:145], v[170:173], v[214:217], v[142:145]
	ds_read_b128 v[214:217], v207 offset:16384
	v_mfma_f32_16x16x32_bf16 v[134:137], v[162:165], v[224:227], v[134:137]
	v_mfma_f32_16x16x32_bf16 v[126:129], v[170:173], v[224:227], v[126:129]
	ds_read_b128 v[224:227], v207 offset:18432
	v_mfma_f32_16x16x32_bf16 v[118:121], v[162:165], v[232:235], v[118:121]
	v_mfma_f32_16x16x32_bf16 v[110:113], v[170:173], v[232:235], v[110:113]
	ds_read_b128 v[232:235], v207 offset:20480
	v_mfma_f32_16x16x32_bf16 v[102:105], v[162:165], v[240:243], v[102:105]
	v_mfma_f32_16x16x32_bf16 v[98:101], v[170:173], v[240:243], v[98:101]
	ds_read_b128 v[240:243], v207 offset:22528
	s_waitcnt lgkmcnt(4)
	v_mfma_f32_16x16x32_bf16 v[150:153], v[166:169], v[218:221], v[150:153]
	v_mfma_f32_16x16x32_bf16 v[142:145], v[174:177], v[218:221], v[142:145]
	ds_read_b128 v[218:221], v207 offset:17408
	v_mfma_f32_16x16x32_bf16 v[134:137], v[166:169], v[228:231], v[134:137]
	v_mfma_f32_16x16x32_bf16 v[126:129], v[174:177], v[228:231], v[126:129]
	ds_read_b128 v[228:231], v207 offset:19456
	v_mfma_f32_16x16x32_bf16 v[118:121], v[166:169], v[236:239], v[118:121]
	v_mfma_f32_16x16x32_bf16 v[110:113], v[174:177], v[236:239], v[110:113]
	ds_read_b128 v[236:239], v207 offset:21504
	v_mfma_f32_16x16x32_bf16 v[102:105], v[166:169], v[244:247], v[102:105]
	v_mfma_f32_16x16x32_bf16 v[98:101], v[174:177], v[244:247], v[98:101]
	ds_read_b128 v[244:247], v207 offset:23552
	s_waitcnt lgkmcnt(7)
	v_mfma_f32_16x16x32_bf16 v[90:93], v[162:165], v[214:217], v[90:93]
	v_mfma_f32_16x16x32_bf16 v[82:85], v[170:173], v[214:217], v[82:85]
	s_waitcnt lgkmcnt(6)
	v_mfma_f32_16x16x32_bf16 v[74:77], v[162:165], v[224:227], v[74:77]
	v_mfma_f32_16x16x32_bf16 v[66:69], v[170:173], v[224:227], v[66:69]
	s_waitcnt lgkmcnt(5)
	v_mfma_f32_16x16x32_bf16 v[58:61], v[162:165], v[232:235], v[58:61]
	v_mfma_f32_16x16x32_bf16 v[50:53], v[170:173], v[232:235], v[50:53]
	s_waitcnt lgkmcnt(4)
	v_mfma_f32_16x16x32_bf16 v[42:45], v[162:165], v[240:243], v[42:45]
	v_mfma_f32_16x16x32_bf16 v[30:33], v[170:173], v[240:243], v[30:33]
	s_waitcnt lgkmcnt(3)
	v_mfma_f32_16x16x32_bf16 v[90:93], v[166:169], v[218:221], v[90:93]
	v_mfma_f32_16x16x32_bf16 v[82:85], v[174:177], v[218:221], v[82:85]
	s_waitcnt lgkmcnt(2)
	v_mfma_f32_16x16x32_bf16 v[74:77], v[166:169], v[228:231], v[74:77]
	v_mfma_f32_16x16x32_bf16 v[66:69], v[174:177], v[228:231], v[66:69]
	s_waitcnt lgkmcnt(1)
	v_mfma_f32_16x16x32_bf16 v[58:61], v[166:169], v[236:239], v[58:61]
	v_mfma_f32_16x16x32_bf16 v[50:53], v[174:177], v[236:239], v[50:53]
	s_waitcnt lgkmcnt(0)
	v_mfma_f32_16x16x32_bf16 v[42:45], v[166:169], v[244:247], v[42:45]
	v_mfma_f32_16x16x32_bf16 v[30:33], v[174:177], v[244:247], v[30:33]
	s_setprio 0

.LBB0_732:
	s_cmp_lg_u64 s[2:3], 0
	s_cbranch_scc1 .Lswp_guO_half
	ds_read_b64_tr_b16 v[162:163], v190 offset:32768
	ds_read_b64_tr_b16 v[164:165], v191 offset:32768
	ds_read_b64_tr_b16 v[166:167], v190 offset:40960
	ds_read_b64_tr_b16 v[168:169], v191 offset:40960
	ds_read_b64_tr_b16 v[170:171], v192 offset:32768
	ds_read_b64_tr_b16 v[172:173], v193 offset:32768
	ds_read_b64_tr_b16 v[174:175], v192 offset:40960
	ds_read_b64_tr_b16 v[176:177], v193 offset:40960
	ds_read_b128 v[214:217], v207 offset:32768
	ds_read_b128 v[224:227], v207 offset:34816
	ds_read_b128 v[232:235], v207 offset:36864
	ds_read_b128 v[240:243], v207 offset:38912
	ds_read_b128 v[218:221], v207 offset:33792
	ds_read_b128 v[228:231], v207 offset:35840
	ds_read_b128 v[236:239], v207 offset:37888
	ds_read_b128 v[244:247], v207 offset:39936
	s_setprio 1
	s_waitcnt lgkmcnt(7)
	v_mfma_f32_16x16x32_bf16 v[158:161], v[162:165], v[214:217], v[158:161]
	v_mfma_f32_16x16x32_bf16 v[154:157], v[170:173], v[214:217], v[154:157]
	ds_read_b128 v[214:217], v207 offset:49152
	s_waitcnt lgkmcnt(7)
	v_mfma_f32_16x16x32_bf16 v[146:149], v[162:165], v[224:227], v[146:149]
	v_mfma_f32_16x16x32_bf16 v[138:141], v[170:173], v[224:227], v[138:141]
	ds_read_b128 v[224:227], v207 offset:51200
	s_waitcnt lgkmcnt(7)
	v_mfma_f32_16x16x32_bf16 v[130:133], v[162:165], v[232:235], v[130:133]
	v_mfma_f32_16x16x32_bf16 v[122:125], v[170:173], v[232:235], v[122:125]
	ds_read_b128 v[232:235], v207 offset:53248
	s_waitcnt lgkmcnt(7)
	v_mfma_f32_16x16x32_bf16 v[114:117], v[162:165], v[240:243], v[114:117]
	v_mfma_f32_16x16x32_bf16 v[106:109], v[170:173], v[240:243], v[106:109]
	ds_read_b128 v[240:243], v207 offset:55296
	s_waitcnt lgkmcnt(7)
	v_mfma_f32_16x16x32_bf16 v[158:161], v[166:169], v[218:221], v[158:161]
	v_mfma_f32_16x16x32_bf16 v[154:157], v[174:177], v[218:221], v[154:157]
	ds_read_b128 v[218:221], v207 offset:50176
	s_waitcnt lgkmcnt(7)
	v_mfma_f32_16x16x32_bf16 v[146:149], v[166:169], v[228:231], v[146:149]
	v_mfma_f32_16x16x32_bf16 v[138:141], v[174:177], v[228:231], v[138:141]
	ds_read_b128 v[228:231], v207 offset:52224
	s_waitcnt lgkmcnt(7)
	v_mfma_f32_16x16x32_bf16 v[130:133], v[166:169], v[236:239], v[130:133]
	v_mfma_f32_16x16x32_bf16 v[122:125], v[174:177], v[236:239], v[122:125]
	ds_read_b128 v[236:239], v207 offset:54272
	s_waitcnt lgkmcnt(7)
	v_mfma_f32_16x16x32_bf16 v[114:117], v[166:169], v[244:247], v[114:117]
	v_mfma_f32_16x16x32_bf16 v[106:109], v[174:177], v[244:247], v[106:109]
	ds_read_b128 v[244:247], v207 offset:56320
	s_waitcnt lgkmcnt(7)
	v_mfma_f32_16x16x32_bf16 v[94:97], v[162:165], v[214:217], v[94:97]
	v_mfma_f32_16x16x32_bf16 v[86:89], v[170:173], v[214:217], v[86:89]
	ds_read_b128 v[214:217], v207 offset:32768
	s_waitcnt lgkmcnt(7)
	v_mfma_f32_16x16x32_bf16 v[78:81], v[162:165], v[224:227], v[78:81]
	v_mfma_f32_16x16x32_bf16 v[70:73], v[170:173], v[224:227], v[70:73]
	ds_read_b128 v[224:227], v207 offset:34816
	s_waitcnt lgkmcnt(7)
	v_mfma_f32_16x16x32_bf16 v[62:65], v[162:165], v[232:235], v[62:65]
	v_mfma_f32_16x16x32_bf16 v[54:57], v[170:173], v[232:235], v[54:57]
	ds_read_b128 v[232:235], v207 offset:36864
	s_waitcnt lgkmcnt(7)
	v_mfma_f32_16x16x32_bf16 v[46:49], v[162:165], v[240:243], v[46:49]
	v_mfma_f32_16x16x32_bf16 v[38:41], v[170:173], v[240:243], v[38:41]
	ds_read_b128 v[240:243], v207 offset:38912
	ds_read_b64_tr_b16 v[162:163], v190 offset:49152
	ds_read_b64_tr_b16 v[164:165], v191 offset:49152
	ds_read_b64_tr_b16 v[170:171], v192 offset:49152
	ds_read_b64_tr_b16 v[172:173], v193 offset:49152
	s_waitcnt lgkmcnt(11)
	v_mfma_f32_16x16x32_bf16 v[94:97], v[166:169], v[218:221], v[94:97]
	v_mfma_f32_16x16x32_bf16 v[86:89], v[174:177], v[218:221], v[86:89]
	ds_read_b128 v[218:221], v207 offset:33792
	s_waitcnt lgkmcnt(11)
	v_mfma_f32_16x16x32_bf16 v[78:81], v[166:169], v[228:231], v[78:81]
	v_mfma_f32_16x16x32_bf16 v[70:73], v[174:177], v[228:231], v[70:73]
	ds_read_b128 v[228:231], v207 offset:35840
	s_waitcnt lgkmcnt(11)
	v_mfma_f32_16x16x32_bf16 v[62:65], v[166:169], v[236:239], v[62:65]
	v_mfma_f32_16x16x32_bf16 v[54:57], v[174:177], v[236:239], v[54:57]
	ds_read_b128 v[236:239], v207 offset:37888
	s_waitcnt lgkmcnt(11)
	v_mfma_f32_16x16x32_bf16 v[46:49], v[166:169], v[244:247], v[46:49]
	v_mfma_f32_16x16x32_bf16 v[38:41], v[174:177], v[244:247], v[38:41]
	ds_read_b128 v[244:247], v207 offset:39936
	ds_read_b64_tr_b16 v[166:167], v190 offset:57344
	ds_read_b64_tr_b16 v[168:169], v191 offset:57344
	ds_read_b64_tr_b16 v[174:175], v192 offset:57344
	ds_read_b64_tr_b16 v[176:177], v193 offset:57344
	s_waitcnt lgkmcnt(8)
	v_mfma_f32_16x16x32_bf16 v[150:153], v[162:165], v[214:217], v[150:153]
	v_mfma_f32_16x16x32_bf16 v[142:145], v[170:173], v[214:217], v[142:145]
	ds_read_b128 v[214:217], v207 offset:49152
	v_mfma_f32_16x16x32_bf16 v[134:137], v[162:165], v[224:227], v[134:137]
	v_mfma_f32_16x16x32_bf16 v[126:129], v[170:173], v[224:227], v[126:129]
	ds_read_b128 v[224:227], v207 offset:51200
	v_mfma_f32_16x16x32_bf16 v[118:121], v[162:165], v[232:235], v[118:121]
	v_mfma_f32_16x16x32_bf16 v[110:113], v[170:173], v[232:235], v[110:113]
	ds_read_b128 v[232:235], v207 offset:53248
	v_mfma_f32_16x16x32_bf16 v[102:105], v[162:165], v[240:243], v[102:105]
	v_mfma_f32_16x16x32_bf16 v[98:101], v[170:173], v[240:243], v[98:101]
	ds_read_b128 v[240:243], v207 offset:55296
	s_waitcnt lgkmcnt(4)
	v_mfma_f32_16x16x32_bf16 v[150:153], v[166:169], v[218:221], v[150:153]
	v_mfma_f32_16x16x32_bf16 v[142:145], v[174:177], v[218:221], v[142:145]
	ds_read_b128 v[218:221], v207 offset:50176
	v_mfma_f32_16x16x32_bf16 v[134:137], v[166:169], v[228:231], v[134:137]
	v_mfma_f32_16x16x32_bf16 v[126:129], v[174:177], v[228:231], v[126:129]
	ds_read_b128 v[228:231], v207 offset:52224
	v_mfma_f32_16x16x32_bf16 v[118:121], v[166:169], v[236:239], v[118:121]
	v_mfma_f32_16x16x32_bf16 v[110:113], v[174:177], v[236:239], v[110:113]
	ds_read_b128 v[236:239], v207 offset:54272
	v_mfma_f32_16x16x32_bf16 v[102:105], v[166:169], v[244:247], v[102:105]
	v_mfma_f32_16x16x32_bf16 v[98:101], v[174:177], v[244:247], v[98:101]
	ds_read_b128 v[244:247], v207 offset:56320
	s_waitcnt lgkmcnt(7)
	v_mfma_f32_16x16x32_bf16 v[90:93], v[162:165], v[214:217], v[90:93]
	v_mfma_f32_16x16x32_bf16 v[82:85], v[170:173], v[214:217], v[82:85]
	s_waitcnt lgkmcnt(6)
	v_mfma_f32_16x16x32_bf16 v[74:77], v[162:165], v[224:227], v[74:77]
	v_mfma_f32_16x16x32_bf16 v[66:69], v[170:173], v[224:227], v[66:69]
	s_waitcnt lgkmcnt(5)
	v_mfma_f32_16x16x32_bf16 v[58:61], v[162:165], v[232:235], v[58:61]
	v_mfma_f32_16x16x32_bf16 v[50:53], v[170:173], v[232:235], v[50:53]
	s_waitcnt lgkmcnt(4)
	v_mfma_f32_16x16x32_bf16 v[42:45], v[162:165], v[240:243], v[42:45]
	v_mfma_f32_16x16x32_bf16 v[30:33], v[170:173], v[240:243], v[30:33]
	s_waitcnt lgkmcnt(3)
	v_mfma_f32_16x16x32_bf16 v[90:93], v[166:169], v[218:221], v[90:93]
	v_mfma_f32_16x16x32_bf16 v[82:85], v[174:177], v[218:221], v[82:85]
	s_waitcnt lgkmcnt(2)
	v_mfma_f32_16x16x32_bf16 v[74:77], v[166:169], v[228:231], v[74:77]
	v_mfma_f32_16x16x32_bf16 v[66:69], v[174:177], v[228:231], v[66:69]
	s_waitcnt lgkmcnt(1)
	v_mfma_f32_16x16x32_bf16 v[58:61], v[166:169], v[236:239], v[58:61]
	v_mfma_f32_16x16x32_bf16 v[50:53], v[174:177], v[236:239], v[50:53]
	s_waitcnt lgkmcnt(0)
	v_mfma_f32_16x16x32_bf16 v[42:45], v[166:169], v[244:247], v[42:45]
	v_mfma_f32_16x16x32_bf16 v[30:33], v[174:177], v[244:247], v[30:33]
	s_setprio 0

.Lwd_guO:
	v_cvt_pk_bf16_f32 v34, v34, v35
	v_cvt_pk_bf16_f32 v35, v36, v37
	ds_write_b64 v194, v[34:35]
	v_cvt_pk_bf16_f32 v22, v22, v23
	v_cvt_pk_bf16_f32 v23, v24, v25
	s_add_u32 s4, s35, s4
	ds_write_b64 v194, v[22:23] offset:16384
	v_cvt_pk_bf16_f32 v22, v26, v27
	v_cvt_pk_bf16_f32 v23, v28, v29
	ds_write_b64 v195, v[22:23]
	v_cvt_pk_bf16_f32 v14, v14, v15
	v_cvt_pk_bf16_f32 v15, v16, v17
	s_addc_u32 s5, s34, s5
	ds_write_b64 v195, v[14:15] offset:16384
	v_cvt_pk_bf16_f32 v14, v18, v19
	v_cvt_pk_bf16_f32 v15, v20, v21
	ds_write_b64 v196, v[14:15]
	v_cvt_pk_bf16_f32 v6, v6, v7
	v_cvt_pk_bf16_f32 v7, v8, v9
	s_add_u32 s34, s2, 0x2000
	ds_write_b64 v196, v[6:7] offset:16384
	v_cvt_pk_bf16_f32 v6, v10, v11
	v_cvt_pk_bf16_f32 v7, v12, v13
	ds_write_b64 v197, v[6:7]
	v_cvt_pk_bf16_f32 v2, v2, v3
	v_cvt_pk_bf16_f32 v3, v4, v5
	ds_write_b64 v197, v[2:3] offset:16384
	s_addc_u32 s35, s3, 0
	global_load_dwordx4 v[2:5], v189, s[2:3]
	s_add_u32 s38, s4, 0x2000
	global_load_dwordx4 v[6:9], v189, s[4:5]
	s_addc_u32 s39, s5, 0
	global_load_dwordx4 v[10:13], v189, s[34:35]
	s_add_u32 s34, s2, 0x4000
	s_addc_u32 s35, s3, 0
	global_load_dwordx4 v[14:17], v189, s[38:39]
	s_add_u32 s38, s4, 0x4000
	s_addc_u32 s39, s5, 0
	global_load_dwordx4 v[18:21], v189, s[34:35]
	s_add_u32 s2, s2, 0x6000
	global_load_dwordx4 v[22:25], v189, s[38:39]
	s_addc_u32 s3, s3, 0
	s_add_u32 s4, s4, 0x6000
	global_load_dwordx4 v[26:29], v189, s[2:3]
	s_addc_u32 s5, s5, 0
	global_load_dwordx4 v[34:37], v189, s[4:5]
	s_waitcnt vmcnt(8)
	s_waitcnt lgkmcnt(0)
	s_barrier
	s_cmp_gt_u32 s17, 29
	s_cbranch_scc1 .LBB0_738
	s_mov_b32 s34, s17
	s_branch .LBB0_724
.Lswp_guE_half:
	ds_read_b64_tr_b16 v[162:163], v190 offset:0
	ds_read_b64_tr_b16 v[164:165], v191 offset:0
	ds_read_b64_tr_b16 v[166:167], v190 offset:8192
	ds_read_b64_tr_b16 v[168:169], v191 offset:8192
	ds_read_b64_tr_b16 v[170:171], v192 offset:0
	ds_read_b64_tr_b16 v[172:173], v193 offset:0
	ds_read_b64_tr_b16 v[174:175], v192 offset:8192
	ds_read_b64_tr_b16 v[176:177], v193 offset:8192
	ds_read_b128 v[214:217], v207
	ds_read_b128 v[218:221], v207 offset:1024
	ds_read_b128 v[224:227], v207 offset:2048
	ds_read_b128 v[228:231], v207 offset:3072
	ds_read_b128 v[232:235], v207 offset:4096
	ds_read_b128 v[236:239], v207 offset:5120
	ds_read_b128 v[240:243], v207 offset:6144
	ds_read_b128 v[244:247], v207 offset:7168
	s_waitcnt lgkmcnt(0)
	s_setprio 1
	s_waitcnt lgkmcnt(0)
	v_mfma_f32_16x16x32_bf16 v[158:161], v[162:165], v[214:217], v[158:161]
	v_mfma_f32_16x16x32_bf16 v[154:157], v[170:173], v[214:217], v[154:157]
	v_mfma_f32_16x16x32_bf16 v[146:149], v[162:165], v[224:227], v[146:149]
	v_mfma_f32_16x16x32_bf16 v[138:141], v[170:173], v[224:227], v[138:141]
	v_mfma_f32_16x16x32_bf16 v[130:133], v[162:165], v[232:235], v[130:133]
	v_mfma_f32_16x16x32_bf16 v[122:125], v[170:173], v[232:235], v[122:125]
	v_mfma_f32_16x16x32_bf16 v[114:117], v[162:165], v[240:243], v[114:117]
	v_mfma_f32_16x16x32_bf16 v[106:109], v[170:173], v[240:243], v[106:109]
	v_mfma_f32_16x16x32_bf16 v[158:161], v[166:169], v[218:221], v[158:161]
	v_mfma_f32_16x16x32_bf16 v[154:157], v[174:177], v[218:221], v[154:157]
	v_mfma_f32_16x16x32_bf16 v[146:149], v[166:169], v[228:231], v[146:149]
	v_mfma_f32_16x16x32_bf16 v[138:141], v[174:177], v[228:231], v[138:141]
	v_mfma_f32_16x16x32_bf16 v[130:133], v[166:169], v[236:239], v[130:133]
	v_mfma_f32_16x16x32_bf16 v[122:125], v[174:177], v[236:239], v[122:125]
	v_mfma_f32_16x16x32_bf16 v[114:117], v[166:169], v[244:247], v[114:117]
	v_mfma_f32_16x16x32_bf16 v[106:109], v[174:177], v[244:247], v[106:109]
	s_setprio 0
	s_and_b64 vcc, exec, s[2:3]
	s_cbranch_vccnz .Lswp_guE_728
	ds_read_b128 v[214:217], v207 offset:16384
	ds_read_b128 v[218:221], v207 offset:17408
	ds_read_b128 v[224:227], v207 offset:18432
	ds_read_b128 v[228:231], v207 offset:19456
	ds_read_b128 v[232:235], v207 offset:20480
	ds_read_b128 v[236:239], v207 offset:21504
	ds_read_b128 v[240:243], v207 offset:22528
	ds_read_b128 v[244:247], v207 offset:23552
	s_waitcnt lgkmcnt(0)
	s_setprio 1
	s_waitcnt lgkmcnt(0)
	v_mfma_f32_16x16x32_bf16 v[94:97], v[162:165], v[214:217], v[94:97]
	v_mfma_f32_16x16x32_bf16 v[86:89], v[170:173], v[214:217], v[86:89]
	v_mfma_f32_16x16x32_bf16 v[78:81], v[162:165], v[224:227], v[78:81]
	v_mfma_f32_16x16x32_bf16 v[70:73], v[170:173], v[224:227], v[70:73]
	v_mfma_f32_16x16x32_bf16 v[62:65], v[162:165], v[232:235], v[62:65]
	v_mfma_f32_16x16x32_bf16 v[54:57], v[170:173], v[232:235], v[54:57]
	v_mfma_f32_16x16x32_bf16 v[46:49], v[162:165], v[240:243], v[46:49]
	v_mfma_f32_16x16x32_bf16 v[38:41], v[170:173], v[240:243], v[38:41]
	v_mfma_f32_16x16x32_bf16 v[94:97], v[166:169], v[218:221], v[94:97]
	v_mfma_f32_16x16x32_bf16 v[86:89], v[174:177], v[218:221], v[86:89]
	v_mfma_f32_16x16x32_bf16 v[78:81], v[166:169], v[228:231], v[78:81]
	v_mfma_f32_16x16x32_bf16 v[70:73], v[174:177], v[228:231], v[70:73]
	v_mfma_f32_16x16x32_bf16 v[62:65], v[166:169], v[236:239], v[62:65]
	v_mfma_f32_16x16x32_bf16 v[54:57], v[174:177], v[236:239], v[54:57]
	v_mfma_f32_16x16x32_bf16 v[46:49], v[166:169], v[244:247], v[46:49]
	v_mfma_f32_16x16x32_bf16 v[38:41], v[174:177], v[244:247], v[38:41]
	s_setprio 0

.Lswp_guE_end:
	s_branch .LBB0_730

.LBB0_858:
	s_cmp_lg_u64 s[2:3], 0
	s_cbranch_scc1 .Lswp_dnE_half
	ds_read_b64_tr_b16 v[164:165], v190 offset:0
	ds_read_b64_tr_b16 v[166:167], v191 offset:0
	ds_read_b64_tr_b16 v[168:169], v190 offset:8192
	ds_read_b64_tr_b16 v[170:171], v191 offset:8192
	ds_read_b64_tr_b16 v[172:173], v192 offset:0
	ds_read_b64_tr_b16 v[174:175], v193 offset:0
	ds_read_b64_tr_b16 v[176:177], v192 offset:8192
	ds_read_b64_tr_b16 v[178:179], v193 offset:8192
	ds_read_b128 v[210:213], v207
	ds_read_b128 v[218:221], v207 offset:2048
	ds_read_b128 v[228:231], v207 offset:4096
	ds_read_b128 v[236:239], v207 offset:6144
	ds_read_b128 v[214:217], v207 offset:1024
	ds_read_b128 v[224:227], v207 offset:3072
	ds_read_b128 v[232:235], v207 offset:5120
	ds_read_b128 v[240:243], v207 offset:7168
	s_setprio 1
	s_waitcnt lgkmcnt(7)
	v_mfma_f32_16x16x32_bf16 v[160:163], v[164:167], v[210:213], v[160:163]
	v_mfma_f32_16x16x32_bf16 v[156:159], v[172:175], v[210:213], v[156:159]
	ds_read_b128 v[210:213], v207 offset:16384
	s_waitcnt lgkmcnt(7)
	v_mfma_f32_16x16x32_bf16 v[152:155], v[164:167], v[218:221], v[152:155]
	v_mfma_f32_16x16x32_bf16 v[148:151], v[172:175], v[218:221], v[148:151]
	ds_read_b128 v[218:221], v207 offset:18432
	s_waitcnt lgkmcnt(7)
	v_mfma_f32_16x16x32_bf16 v[136:139], v[164:167], v[228:231], v[136:139]
	v_mfma_f32_16x16x32_bf16 v[132:135], v[172:175], v[228:231], v[132:135]
	ds_read_b128 v[228:231], v207 offset:20480
	s_waitcnt lgkmcnt(7)
	v_mfma_f32_16x16x32_bf16 v[120:123], v[164:167], v[236:239], v[120:123]
	v_mfma_f32_16x16x32_bf16 v[116:119], v[172:175], v[236:239], v[116:119]
	ds_read_b128 v[236:239], v207 offset:22528
	s_waitcnt lgkmcnt(7)
	v_mfma_f32_16x16x32_bf16 v[160:163], v[168:171], v[214:217], v[160:163]
	v_mfma_f32_16x16x32_bf16 v[156:159], v[176:179], v[214:217], v[156:159]
	ds_read_b128 v[214:217], v207 offset:17408
	s_waitcnt lgkmcnt(7)
	v_mfma_f32_16x16x32_bf16 v[152:155], v[168:171], v[224:227], v[152:155]
	v_mfma_f32_16x16x32_bf16 v[148:151], v[176:179], v[224:227], v[148:151]
	ds_read_b128 v[224:227], v207 offset:19456
	s_waitcnt lgkmcnt(7)
	v_mfma_f32_16x16x32_bf16 v[136:139], v[168:171], v[232:235], v[136:139]
	v_mfma_f32_16x16x32_bf16 v[132:135], v[176:179], v[232:235], v[132:135]
	ds_read_b128 v[232:235], v207 offset:21504
	s_waitcnt lgkmcnt(7)
	v_mfma_f32_16x16x32_bf16 v[120:123], v[168:171], v[240:243], v[120:123]
	v_mfma_f32_16x16x32_bf16 v[116:119], v[176:179], v[240:243], v[116:119]
	ds_read_b128 v[240:243], v207 offset:23552
	s_waitcnt lgkmcnt(7)
	v_mfma_f32_16x16x32_bf16 v[80:83], v[164:167], v[210:213], v[80:83]
	v_mfma_f32_16x16x32_bf16 v[68:71], v[172:175], v[210:213], v[68:71]
	ds_read_b128 v[210:213], v207
	s_waitcnt lgkmcnt(7)
	v_mfma_f32_16x16x32_bf16 v[48:51], v[164:167], v[218:221], v[48:51]
	v_mfma_f32_16x16x32_bf16 v[44:47], v[172:175], v[218:221], v[44:47]
	ds_read_b128 v[218:221], v207 offset:2048
	s_waitcnt lgkmcnt(7)
	v_mfma_f32_16x16x32_bf16 v[32:35], v[164:167], v[228:231], v[32:35]
	v_mfma_f32_16x16x32_bf16 v[28:31], v[172:175], v[228:231], v[28:31]
	ds_read_b128 v[228:231], v207 offset:4096
	s_waitcnt lgkmcnt(7)
	v_mfma_f32_16x16x32_bf16 v[16:19], v[164:167], v[236:239], v[16:19]
	v_mfma_f32_16x16x32_bf16 v[12:15], v[172:175], v[236:239], v[12:15]
	ds_read_b128 v[236:239], v207 offset:6144
	ds_read_b64_tr_b16 v[164:165], v190 offset:16384
	ds_read_b64_tr_b16 v[166:167], v191 offset:16384
	ds_read_b64_tr_b16 v[172:173], v192 offset:16384
	ds_read_b64_tr_b16 v[174:175], v193 offset:16384
	s_waitcnt lgkmcnt(11)
	v_mfma_f32_16x16x32_bf16 v[80:83], v[168:171], v[214:217], v[80:83]
	v_mfma_f32_16x16x32_bf16 v[68:71], v[176:179], v[214:217], v[68:71]
	ds_read_b128 v[214:217], v207 offset:1024
	s_waitcnt lgkmcnt(11)
	v_mfma_f32_16x16x32_bf16 v[48:51], v[168:171], v[224:227], v[48:51]
	v_mfma_f32_16x16x32_bf16 v[44:47], v[176:179], v[224:227], v[44:47]
	ds_read_b128 v[224:227], v207 offset:3072
	s_waitcnt lgkmcnt(11)
	v_mfma_f32_16x16x32_bf16 v[32:35], v[168:171], v[232:235], v[32:35]
	v_mfma_f32_16x16x32_bf16 v[28:31], v[176:179], v[232:235], v[28:31]
	ds_read_b128 v[232:235], v207 offset:5120
	s_waitcnt lgkmcnt(11)
	v_mfma_f32_16x16x32_bf16 v[16:19], v[168:171], v[240:243], v[16:19]
	v_mfma_f32_16x16x32_bf16 v[12:15], v[176:179], v[240:243], v[12:15]
	ds_read_b128 v[240:243], v207 offset:7168
	ds_read_b64_tr_b16 v[168:169], v190 offset:24576
	ds_read_b64_tr_b16 v[170:171], v191 offset:24576
	ds_read_b64_tr_b16 v[176:177], v192 offset:24576
	ds_read_b64_tr_b16 v[178:179], v193 offset:24576
	s_waitcnt lgkmcnt(8)
	v_mfma_f32_16x16x32_bf16 v[144:147], v[164:167], v[210:213], v[144:147]
	v_mfma_f32_16x16x32_bf16 v[140:143], v[172:175], v[210:213], v[140:143]
	ds_read_b128 v[210:213], v207 offset:16384
	v_mfma_f32_16x16x32_bf16 v[128:131], v[164:167], v[218:221], v[128:131]
	v_mfma_f32_16x16x32_bf16 v[124:127], v[172:175], v[218:221], v[124:127]
	ds_read_b128 v[218:221], v207 offset:18432
	v_mfma_f32_16x16x32_bf16 v[112:115], v[164:167], v[228:231], v[112:115]
	v_mfma_f32_16x16x32_bf16 v[108:111], v[172:175], v[228:231], v[108:111]
	ds_read_b128 v[228:231], v207 offset:20480
	v_mfma_f32_16x16x32_bf16 v[104:107], v[164:167], v[236:239], v[104:107]
	v_mfma_f32_16x16x32_bf16 v[100:103], v[172:175], v[236:239], v[100:103]
	ds_read_b128 v[236:239], v207 offset:22528
	s_waitcnt lgkmcnt(4)
	v_mfma_f32_16x16x32_bf16 v[144:147], v[168:171], v[214:217], v[144:147]
	v_mfma_f32_16x16x32_bf16 v[140:143], v[176:179], v[214:217], v[140:143]
	ds_read_b128 v[214:217], v207 offset:17408
	v_mfma_f32_16x16x32_bf16 v[128:131], v[168:171], v[224:227], v[128:131]
	v_mfma_f32_16x16x32_bf16 v[124:127], v[176:179], v[224:227], v[124:127]
	ds_read_b128 v[224:227], v207 offset:19456
	v_mfma_f32_16x16x32_bf16 v[112:115], v[168:171], v[232:235], v[112:115]
	v_mfma_f32_16x16x32_bf16 v[108:111], v[176:179], v[232:235], v[108:111]
	ds_read_b128 v[232:235], v207 offset:21504
	v_mfma_f32_16x16x32_bf16 v[104:107], v[168:171], v[240:243], v[104:107]
	v_mfma_f32_16x16x32_bf16 v[100:103], v[176:179], v[240:243], v[100:103]
	ds_read_b128 v[240:243], v207 offset:23552
	s_waitcnt lgkmcnt(7)
	v_mfma_f32_16x16x32_bf16 v[56:59], v[164:167], v[210:213], v[56:59]
	v_mfma_f32_16x16x32_bf16 v[52:55], v[172:175], v[210:213], v[52:55]
	s_waitcnt lgkmcnt(6)
	v_mfma_f32_16x16x32_bf16 v[40:43], v[164:167], v[218:221], v[40:43]
	v_mfma_f32_16x16x32_bf16 v[36:39], v[172:175], v[218:221], v[36:39]
	s_waitcnt lgkmcnt(5)
	v_mfma_f32_16x16x32_bf16 v[24:27], v[164:167], v[228:231], v[24:27]
	v_mfma_f32_16x16x32_bf16 v[20:23], v[172:175], v[228:231], v[20:23]
	s_waitcnt lgkmcnt(4)
	v_mfma_f32_16x16x32_bf16 v[8:11], v[164:167], v[236:239], v[8:11]
	v_mfma_f32_16x16x32_bf16 v[2:5], v[172:175], v[236:239], v[4:7]
	s_waitcnt lgkmcnt(3)
	v_mfma_f32_16x16x32_bf16 v[56:59], v[168:171], v[214:217], v[56:59]
	v_mfma_f32_16x16x32_bf16 v[52:55], v[176:179], v[214:217], v[52:55]
	s_waitcnt lgkmcnt(2)
	v_mfma_f32_16x16x32_bf16 v[40:43], v[168:171], v[224:227], v[40:43]
	v_mfma_f32_16x16x32_bf16 v[36:39], v[176:179], v[224:227], v[36:39]
	s_waitcnt lgkmcnt(1)
	v_mfma_f32_16x16x32_bf16 v[24:27], v[168:171], v[232:235], v[24:27]
	v_mfma_f32_16x16x32_bf16 v[20:23], v[176:179], v[232:235], v[20:23]
	s_waitcnt lgkmcnt(0)
	v_mfma_f32_16x16x32_bf16 v[8:11], v[168:171], v[240:243], v[8:11]
	v_mfma_f32_16x16x32_bf16 v[4:7], v[176:179], v[240:243], v[2:5]
	s_setprio 0

.LBB0_864:
	s_cmp_lg_u64 s[2:3], 0
	s_cbranch_scc1 .Lswp_dnO_half
	ds_read_b64_tr_b16 v[164:165], v190 offset:32768
	ds_read_b64_tr_b16 v[166:167], v191 offset:32768
	ds_read_b64_tr_b16 v[168:169], v190 offset:40960
	ds_read_b64_tr_b16 v[170:171], v191 offset:40960
	ds_read_b64_tr_b16 v[172:173], v192 offset:32768
	ds_read_b64_tr_b16 v[174:175], v193 offset:32768
	ds_read_b64_tr_b16 v[176:177], v192 offset:40960
	ds_read_b64_tr_b16 v[178:179], v193 offset:40960
	ds_read_b128 v[210:213], v207 offset:32768
	ds_read_b128 v[218:221], v207 offset:34816
	ds_read_b128 v[228:231], v207 offset:36864
	ds_read_b128 v[236:239], v207 offset:38912
	ds_read_b128 v[214:217], v207 offset:33792
	ds_read_b128 v[224:227], v207 offset:35840
	ds_read_b128 v[232:235], v207 offset:37888
	ds_read_b128 v[240:243], v207 offset:39936
	s_setprio 1
	s_waitcnt lgkmcnt(7)
	v_mfma_f32_16x16x32_bf16 v[160:163], v[164:167], v[210:213], v[160:163]
	v_mfma_f32_16x16x32_bf16 v[156:159], v[172:175], v[210:213], v[156:159]
	ds_read_b128 v[210:213], v207 offset:49152
	s_waitcnt lgkmcnt(7)
	v_mfma_f32_16x16x32_bf16 v[152:155], v[164:167], v[218:221], v[152:155]
	v_mfma_f32_16x16x32_bf16 v[148:151], v[172:175], v[218:221], v[148:151]
	ds_read_b128 v[218:221], v207 offset:51200
	s_waitcnt lgkmcnt(7)
	v_mfma_f32_16x16x32_bf16 v[136:139], v[164:167], v[228:231], v[136:139]
	v_mfma_f32_16x16x32_bf16 v[132:135], v[172:175], v[228:231], v[132:135]
	ds_read_b128 v[228:231], v207 offset:53248
	s_waitcnt lgkmcnt(7)
	v_mfma_f32_16x16x32_bf16 v[120:123], v[164:167], v[236:239], v[120:123]
	v_mfma_f32_16x16x32_bf16 v[116:119], v[172:175], v[236:239], v[116:119]
	ds_read_b128 v[236:239], v207 offset:55296
	s_waitcnt lgkmcnt(7)
	v_mfma_f32_16x16x32_bf16 v[160:163], v[168:171], v[214:217], v[160:163]
	v_mfma_f32_16x16x32_bf16 v[156:159], v[176:179], v[214:217], v[156:159]
	ds_read_b128 v[214:217], v207 offset:50176
	s_waitcnt lgkmcnt(7)
	v_mfma_f32_16x16x32_bf16 v[152:155], v[168:171], v[224:227], v[152:155]
	v_mfma_f32_16x16x32_bf16 v[148:151], v[176:179], v[224:227], v[148:151]
	ds_read_b128 v[224:227], v207 offset:52224
	s_waitcnt lgkmcnt(7)
	v_mfma_f32_16x16x32_bf16 v[136:139], v[168:171], v[232:235], v[136:139]
	v_mfma_f32_16x16x32_bf16 v[132:135], v[176:179], v[232:235], v[132:135]
	ds_read_b128 v[232:235], v207 offset:54272
	s_waitcnt lgkmcnt(7)
	v_mfma_f32_16x16x32_bf16 v[120:123], v[168:171], v[240:243], v[120:123]
	v_mfma_f32_16x16x32_bf16 v[116:119], v[176:179], v[240:243], v[116:119]
	ds_read_b128 v[240:243], v207 offset:56320
	s_waitcnt lgkmcnt(7)
	v_mfma_f32_16x16x32_bf16 v[80:83], v[164:167], v[210:213], v[80:83]
	v_mfma_f32_16x16x32_bf16 v[68:71], v[172:175], v[210:213], v[68:71]
	ds_read_b128 v[210:213], v207 offset:32768
	s_waitcnt lgkmcnt(7)
	v_mfma_f32_16x16x32_bf16 v[48:51], v[164:167], v[218:221], v[48:51]
	v_mfma_f32_16x16x32_bf16 v[44:47], v[172:175], v[218:221], v[44:47]
	ds_read_b128 v[218:221], v207 offset:34816
	s_waitcnt lgkmcnt(7)
	v_mfma_f32_16x16x32_bf16 v[32:35], v[164:167], v[228:231], v[32:35]
	v_mfma_f32_16x16x32_bf16 v[28:31], v[172:175], v[228:231], v[28:31]
	ds_read_b128 v[228:231], v207 offset:36864
	s_waitcnt lgkmcnt(7)
	v_mfma_f32_16x16x32_bf16 v[16:19], v[164:167], v[236:239], v[16:19]
	v_mfma_f32_16x16x32_bf16 v[12:15], v[172:175], v[236:239], v[12:15]
	ds_read_b128 v[236:239], v207 offset:38912
	ds_read_b64_tr_b16 v[164:165], v190 offset:49152
	ds_read_b64_tr_b16 v[166:167], v191 offset:49152
	ds_read_b64_tr_b16 v[172:173], v192 offset:49152
	ds_read_b64_tr_b16 v[174:175], v193 offset:49152
	s_waitcnt lgkmcnt(11)
	v_mfma_f32_16x16x32_bf16 v[80:83], v[168:171], v[214:217], v[80:83]
	v_mfma_f32_16x16x32_bf16 v[68:71], v[176:179], v[214:217], v[68:71]
	ds_read_b128 v[214:217], v207 offset:33792
	s_waitcnt lgkmcnt(11)
	v_mfma_f32_16x16x32_bf16 v[48:51], v[168:171], v[224:227], v[48:51]
	v_mfma_f32_16x16x32_bf16 v[44:47], v[176:179], v[224:227], v[44:47]
	ds_read_b128 v[224:227], v207 offset:35840
	s_waitcnt lgkmcnt(11)
	v_mfma_f32_16x16x32_bf16 v[32:35], v[168:171], v[232:235], v[32:35]
	v_mfma_f32_16x16x32_bf16 v[28:31], v[176:179], v[232:235], v[28:31]
	ds_read_b128 v[232:235], v207 offset:37888
	s_waitcnt lgkmcnt(11)
	v_mfma_f32_16x16x32_bf16 v[16:19], v[168:171], v[240:243], v[16:19]
	v_mfma_f32_16x16x32_bf16 v[12:15], v[176:179], v[240:243], v[12:15]
	ds_read_b128 v[240:243], v207 offset:39936
	ds_read_b64_tr_b16 v[168:169], v190 offset:57344
	ds_read_b64_tr_b16 v[170:171], v191 offset:57344
	ds_read_b64_tr_b16 v[176:177], v192 offset:57344
	ds_read_b64_tr_b16 v[178:179], v193 offset:57344
	s_waitcnt lgkmcnt(8)
	v_mfma_f32_16x16x32_bf16 v[144:147], v[164:167], v[210:213], v[144:147]
	v_mfma_f32_16x16x32_bf16 v[140:143], v[172:175], v[210:213], v[140:143]
	ds_read_b128 v[210:213], v207 offset:49152
	v_mfma_f32_16x16x32_bf16 v[128:131], v[164:167], v[218:221], v[128:131]
	v_mfma_f32_16x16x32_bf16 v[124:127], v[172:175], v[218:221], v[124:127]
	ds_read_b128 v[218:221], v207 offset:51200
	v_mfma_f32_16x16x32_bf16 v[112:115], v[164:167], v[228:231], v[112:115]
	v_mfma_f32_16x16x32_bf16 v[108:111], v[172:175], v[228:231], v[108:111]
	ds_read_b128 v[228:231], v207 offset:53248
	v_mfma_f32_16x16x32_bf16 v[104:107], v[164:167], v[236:239], v[104:107]
	v_mfma_f32_16x16x32_bf16 v[100:103], v[172:175], v[236:239], v[100:103]
	ds_read_b128 v[236:239], v207 offset:55296
	s_waitcnt lgkmcnt(4)
	v_mfma_f32_16x16x32_bf16 v[144:147], v[168:171], v[214:217], v[144:147]
	v_mfma_f32_16x16x32_bf16 v[140:143], v[176:179], v[214:217], v[140:143]
	ds_read_b128 v[214:217], v207 offset:50176
	v_mfma_f32_16x16x32_bf16 v[128:131], v[168:171], v[224:227], v[128:131]
	v_mfma_f32_16x16x32_bf16 v[124:127], v[176:179], v[224:227], v[124:127]
	ds_read_b128 v[224:227], v207 offset:52224
	v_mfma_f32_16x16x32_bf16 v[112:115], v[168:171], v[232:235], v[112:115]
	v_mfma_f32_16x16x32_bf16 v[108:111], v[176:179], v[232:235], v[108:111]
	ds_read_b128 v[232:235], v207 offset:54272
	v_mfma_f32_16x16x32_bf16 v[104:107], v[168:171], v[240:243], v[104:107]
	v_mfma_f32_16x16x32_bf16 v[100:103], v[176:179], v[240:243], v[100:103]
	ds_read_b128 v[240:243], v207 offset:56320
	s_waitcnt lgkmcnt(7)
	v_mfma_f32_16x16x32_bf16 v[56:59], v[164:167], v[210:213], v[56:59]
	v_mfma_f32_16x16x32_bf16 v[52:55], v[172:175], v[210:213], v[52:55]
	s_waitcnt lgkmcnt(6)
	v_mfma_f32_16x16x32_bf16 v[40:43], v[164:167], v[218:221], v[40:43]
	v_mfma_f32_16x16x32_bf16 v[36:39], v[172:175], v[218:221], v[36:39]
	s_waitcnt lgkmcnt(5)
	v_mfma_f32_16x16x32_bf16 v[24:27], v[164:167], v[228:231], v[24:27]
	v_mfma_f32_16x16x32_bf16 v[20:23], v[172:175], v[228:231], v[20:23]
	s_waitcnt lgkmcnt(4)
	v_mfma_f32_16x16x32_bf16 v[8:11], v[164:167], v[236:239], v[8:11]
	v_mfma_f32_16x16x32_bf16 v[2:5], v[172:175], v[236:239], v[4:7]
	s_waitcnt lgkmcnt(3)
	v_mfma_f32_16x16x32_bf16 v[56:59], v[168:171], v[214:217], v[56:59]
	v_mfma_f32_16x16x32_bf16 v[52:55], v[176:179], v[214:217], v[52:55]
	s_waitcnt lgkmcnt(2)
	v_mfma_f32_16x16x32_bf16 v[40:43], v[168:171], v[224:227], v[40:43]
	v_mfma_f32_16x16x32_bf16 v[36:39], v[176:179], v[224:227], v[36:39]
	s_waitcnt lgkmcnt(1)
	v_mfma_f32_16x16x32_bf16 v[24:27], v[168:171], v[232:235], v[24:27]
	v_mfma_f32_16x16x32_bf16 v[20:23], v[176:179], v[232:235], v[20:23]
	s_waitcnt lgkmcnt(0)
	v_mfma_f32_16x16x32_bf16 v[8:11], v[168:171], v[240:243], v[8:11]
	v_mfma_f32_16x16x32_bf16 v[4:7], v[176:179], v[240:243], v[2:5]
	s_setprio 0

.Lwd_dnO:
	s_add_u32 s48, s2, 0x80000
	v_cvt_pk_bf16_f32 v2, v96, v97
	v_cvt_pk_bf16_f32 v3, v98, v99
	ds_write_b64 v194, v[2:3]
	v_cvt_pk_bf16_f32 v2, v88, v89
	v_cvt_pk_bf16_f32 v3, v90, v91
	s_addc_u32 s49, s3, 0
	ds_write_b64 v194, v[2:3] offset:16384
	v_cvt_pk_bf16_f32 v2, v92, v93
	v_cvt_pk_bf16_f32 v3, v94, v95
	s_add_u32 s2, s74, s48
	ds_write_b64 v195, v[2:3]
	v_cvt_pk_bf16_f32 v2, v76, v77
	v_cvt_pk_bf16_f32 v3, v78, v79
	s_addc_u32 s3, s43, s49
	ds_write_b64 v195, v[2:3] offset:16384
	v_cvt_pk_bf16_f32 v2, v84, v85
	v_cvt_pk_bf16_f32 v3, v86, v87
	s_add_u32 s48, s37, s48
	ds_write_b64 v196, v[2:3]
	v_cvt_pk_bf16_f32 v2, v64, v65
	v_cvt_pk_bf16_f32 v3, v66, v67
	s_addc_u32 s49, s35, s49
	ds_write_b64 v196, v[2:3] offset:16384
	v_cvt_pk_bf16_f32 v2, v72, v73
	v_cvt_pk_bf16_f32 v3, v74, v75
	s_add_u32 s50, s2, 0x4000
	ds_write_b64 v197, v[2:3]
	v_cvt_pk_bf16_f32 v2, v60, v61
	v_cvt_pk_bf16_f32 v3, v62, v63
	ds_write_b64 v197, v[2:3] offset:16384
	s_addc_u32 s51, s3, 0
	global_load_dwordx4 v[64:67], v189, s[2:3]
	s_add_u32 s72, s48, 0x4000
	global_load_dwordx4 v[60:63], v189, s[48:49]
	s_addc_u32 s73, s49, 0
	global_load_dwordx4 v[76:79], v189, s[50:51]
	s_add_u32 s50, s2, 0x8000
	s_addc_u32 s51, s3, 0
	global_load_dwordx4 v[72:75], v189, s[72:73]
	s_add_u32 s72, s48, 0x8000
	s_addc_u32 s73, s49, 0
	global_load_dwordx4 v[88:91], v189, s[50:51]
	s_add_u32 s2, s2, 0xc000
	global_load_dwordx4 v[84:87], v189, s[72:73]
	s_addc_u32 s3, s3, 0
	s_add_u32 s48, s48, 0xc000
	global_load_dwordx4 v[96:99], v189, s[2:3]
	s_addc_u32 s49, s49, 0
	global_load_dwordx4 v[92:95], v189, s[48:49]
	s_waitcnt vmcnt(8)
	s_waitcnt lgkmcnt(0)
	s_barrier
	s_cmp_gt_u32 s34, 13
	s_cbranch_scc1 .LBB0_870
	s_mov_b32 s35, s34
	s_branch .LBB0_856
.Lswp_dnE_half:
	ds_read_b64_tr_b16 v[164:165], v190 offset:0
	ds_read_b64_tr_b16 v[166:167], v191 offset:0
	ds_read_b64_tr_b16 v[168:169], v190 offset:8192
	ds_read_b64_tr_b16 v[170:171], v191 offset:8192
	ds_read_b64_tr_b16 v[172:173], v192 offset:0
	ds_read_b64_tr_b16 v[174:175], v193 offset:0
	ds_read_b64_tr_b16 v[176:177], v192 offset:8192
	ds_read_b64_tr_b16 v[178:179], v193 offset:8192
	ds_read_b128 v[210:213], v207
	ds_read_b128 v[214:217], v207 offset:1024
	ds_read_b128 v[218:221], v207 offset:2048
	ds_read_b128 v[224:227], v207 offset:3072
	ds_read_b128 v[228:231], v207 offset:4096
	ds_read_b128 v[232:235], v207 offset:5120
	ds_read_b128 v[236:239], v207 offset:6144
	ds_read_b128 v[240:243], v207 offset:7168
	s_waitcnt lgkmcnt(0)
	s_setprio 1
	s_waitcnt lgkmcnt(0)
	v_mfma_f32_16x16x32_bf16 v[160:163], v[164:167], v[210:213], v[160:163]
	v_mfma_f32_16x16x32_bf16 v[156:159], v[172:175], v[210:213], v[156:159]
	v_mfma_f32_16x16x32_bf16 v[152:155], v[164:167], v[218:221], v[152:155]
	v_mfma_f32_16x16x32_bf16 v[148:151], v[172:175], v[218:221], v[148:151]
	v_mfma_f32_16x16x32_bf16 v[136:139], v[164:167], v[228:231], v[136:139]
	v_mfma_f32_16x16x32_bf16 v[132:135], v[172:175], v[228:231], v[132:135]
	v_mfma_f32_16x16x32_bf16 v[120:123], v[164:167], v[236:239], v[120:123]
	v_mfma_f32_16x16x32_bf16 v[116:119], v[172:175], v[236:239], v[116:119]
	v_mfma_f32_16x16x32_bf16 v[160:163], v[168:171], v[214:217], v[160:163]
	v_mfma_f32_16x16x32_bf16 v[156:159], v[176:179], v[214:217], v[156:159]
	v_mfma_f32_16x16x32_bf16 v[152:155], v[168:171], v[224:227], v[152:155]
	v_mfma_f32_16x16x32_bf16 v[148:151], v[176:179], v[224:227], v[148:151]
	v_mfma_f32_16x16x32_bf16 v[136:139], v[168:171], v[232:235], v[136:139]
	v_mfma_f32_16x16x32_bf16 v[132:135], v[176:179], v[232:235], v[132:135]
	v_mfma_f32_16x16x32_bf16 v[120:123], v[168:171], v[240:243], v[120:123]
	v_mfma_f32_16x16x32_bf16 v[116:119], v[176:179], v[240:243], v[116:119]
	s_setprio 0
	s_and_b64 vcc, exec, s[2:3]
	s_cbranch_vccnz .Lswp_dnE_860
	ds_read_b128 v[210:213], v207 offset:16384
	ds_read_b128 v[214:217], v207 offset:17408
	ds_read_b128 v[218:221], v207 offset:18432
	ds_read_b128 v[224:227], v207 offset:19456
	ds_read_b128 v[228:231], v207 offset:20480
	ds_read_b128 v[232:235], v207 offset:21504
	ds_read_b128 v[236:239], v207 offset:22528
	ds_read_b128 v[240:243], v207 offset:23552
	s_waitcnt lgkmcnt(0)
	s_setprio 1
	s_waitcnt lgkmcnt(0)
	v_mfma_f32_16x16x32_bf16 v[80:83], v[164:167], v[210:213], v[80:83]
	v_mfma_f32_16x16x32_bf16 v[68:71], v[172:175], v[210:213], v[68:71]
	v_mfma_f32_16x16x32_bf16 v[48:51], v[164:167], v[218:221], v[48:51]
	v_mfma_f32_16x16x32_bf16 v[44:47], v[172:175], v[218:221], v[44:47]
	v_mfma_f32_16x16x32_bf16 v[32:35], v[164:167], v[228:231], v[32:35]
	v_mfma_f32_16x16x32_bf16 v[28:31], v[172:175], v[228:231], v[28:31]
	v_mfma_f32_16x16x32_bf16 v[16:19], v[164:167], v[236:239], v[16:19]
	v_mfma_f32_16x16x32_bf16 v[12:15], v[172:175], v[236:239], v[12:15]
	v_mfma_f32_16x16x32_bf16 v[80:83], v[168:171], v[214:217], v[80:83]
	v_mfma_f32_16x16x32_bf16 v[68:71], v[176:179], v[214:217], v[68:71]
	v_mfma_f32_16x16x32_bf16 v[48:51], v[168:171], v[224:227], v[48:51]
	v_mfma_f32_16x16x32_bf16 v[44:47], v[176:179], v[224:227], v[44:47]
	v_mfma_f32_16x16x32_bf16 v[32:35], v[168:171], v[232:235], v[32:35]
	v_mfma_f32_16x16x32_bf16 v[28:31], v[176:179], v[232:235], v[28:31]
	v_mfma_f32_16x16x32_bf16 v[16:19], v[168:171], v[240:243], v[16:19]
	v_mfma_f32_16x16x32_bf16 v[12:15], v[176:179], v[240:243], v[12:15]
	s_setprio 0
